# prologue row conversion software-pipelined over rows: next row's four loads issued at the top of the current row, source pointers read once before the loop
# baseline (speedup 1.0000x reference)
; #define GAS __attribute__((address_space(1)))
; __device__ __forceinline__ void p0_prologue(Frame& F, KArgs A) {
;     ...
;     for (int m = gw; m < M + 1024; m += NGW) {
;         const bool ismem = m >= M; const int row = ismem ? m - M : m;
;         const GAS f32x4* xr = (const GAS f32x4*)((ismem ? INF(A, I_MEM) : INF(A, I_X)) + (size_t)row * D) + lane;
;         GAS unsigned long long* o8 = (GAS unsigned long long*)((bf16*)(ws + (ismem ? WS_MK : WS_X)) + (size_t)row * D) + lane;
.LBB0_351:
	s_cmp_gt_i32 s3, 0x83ff
	s_cbranch_scc1 .LBB0_362
	v_mov_b32_e32 v5, 0
	v_lshlrev_b32_e32 v4, 2, v2
	s_waitcnt lgkmcnt(0)
	v_lshl_add_u64 v[6:7], s[12:13], 0, v[4:5]
	v_mbcnt_lo_u32_b32 v4, -1, 0
	v_mbcnt_hi_u32_b32 v12, -1, v4
	v_and_b32_e32 v4, 64, v12
	v_add_u32_e32 v13, 64, v4
	v_xor_b32_e32 v4, 1, v12
	v_cmp_lt_i32_e32 vcc, v4, v13
	v_xor_b32_e32 v8, 2, v12
	v_xor_b32_e32 v9, 4, v12
	v_cndmask_b32_e32 v4, v12, v4, vcc
	v_cmp_lt_i32_e32 vcc, v8, v13
	v_xor_b32_e32 v10, 8, v12
	v_xor_b32_e32 v11, 16, v12
	v_cndmask_b32_e32 v8, v12, v8, vcc
	v_cmp_lt_i32_e32 vcc, v9, v13
	v_xor_b32_e32 v14, 32, v12
	s_mov_b64 s[4:5], 0x1c000000
	v_cndmask_b32_e32 v9, v12, v9, vcc
	v_cmp_lt_i32_e32 vcc, v10, v13
	s_add_u32 s18, s12, 0x300000
	v_cmp_gt_u32_e64 s[6:7], 16, v2
	v_cndmask_b32_e32 v10, v12, v10, vcc
	v_cmp_lt_i32_e32 vcc, v11, v13
	v_lshl_add_u64 v[6:7], v[6:7], 0, s[4:5]
	v_cmp_eq_u32_e64 s[4:5], 0, v2
	v_cndmask_b32_e32 v11, v12, v11, vcc
	v_cmp_lt_i32_e32 vcc, v14, v13
	s_addc_u32 s19, s13, 0
	v_lshlrev_b32_e32 v4, 2, v4
	v_cndmask_b32_e32 v12, v12, v14, vcc
	v_lshlrev_b32_e32 v8, 2, v8
	v_lshlrev_b32_e32 v9, 2, v9
	v_lshlrev_b32_e32 v10, 2, v10
	v_lshlrev_b32_e32 v11, 2, v11
	v_lshlrev_b32_e32 v12, 2, v12
	s_movk_i32 s20, 0x7fff
	s_mov_b32 s21, 0xc00000
	v_lshlrev_b32_e32 v13, 4, v2
	v_lshlrev_b32_e32 v2, 3, v2
	s_load_dwordx2 s[34:35], s[14:15], 0x0
	s_load_dwordx2 s[36:37], s[14:15], 0x8
	s_waitcnt lgkmcnt(0)
	s_add_i32 s40, s3, 0xffff8000
	s_cmpk_gt_i32 s3, 0x7fff
	s_cselect_b32 s40, s40, s3
	s_cselect_b32 s42, s36, s34
	s_cselect_b32 s43, s37, s35
	s_ashr_i32 s41, s40, 31
	s_lshl_b64 s[40:41], s[40:41], 12
	s_add_u32 s16, s42, s40
	s_addc_u32 s17, s43, s41
	global_load_dwordx4 v[44:47], v13, s[16:17]
	global_load_dwordx4 v[48:51], v13, s[16:17] offset:1024
	global_load_dwordx4 v[52:55], v13, s[16:17] offset:2048
	global_load_dwordx4 v[56:59], v13, s[16:17] offset:3072
	s_waitcnt vmcnt(0)
	s_branch .LBB0_355

; #define GAS __attribute__((address_space(1)))
; __device__ __forceinline__ unsigned pk2(float lo, float hi) { return f2bf(lo) | (f2bf(hi) << 16); }
; __device__ __forceinline__ float bf2f_lo(unsigned w) { return __uint_as_float(w << 16); }
; __device__ __forceinline__ float bf2f_hi(unsigned w) { return __uint_as_float(w & 0xffff0000u); }
; __device__ __forceinline__ void p0_prologue(Frame& F, KArgs A) {
;     ...
;     for (int m = gw; m < M + 1024; m += NGW) {
;         const bool ismem = m >= M; const int row = ismem ? m - M : m;
;         const GAS f32x4* xr = (const GAS f32x4*)((ismem ? INF(A, I_MEM) : INF(A, I_X)) + (size_t)row * D) + lane;
;         GAS unsigned long long* o8 = (GAS unsigned long long*)((bf16*)(ws + (ismem ? WS_MK : WS_X)) + (size_t)row * D) + lane;
;         float s = 0.f;
; #pragma unroll
;         for (int j = 0; j < 4; ++j) { const f32x4 v = xr[64 * j]; const unsigned a = pk2(v.x, v.y), b = pk2(v.z, v.w); o8[64 * j] = (unsigned long long)a | ((unsigned long long)b << 32);
;             s += (bf2f_lo(a) * bf2f_lo(a) + bf2f_hi(a) * bf2f_hi(a)) + (bf2f_lo(b) * bf2f_lo(b) + bf2f_hi(b) * bf2f_hi(b)); }
.LBB0_355:
	s_waitcnt vmcnt(5)
	v_mov_b64_e32 v[14:15], v[44:45]
	v_mov_b64_e32 v[16:17], v[46:47]
	v_mov_b64_e32 v[32:33], v[48:49]
	v_mov_b64_e32 v[34:35], v[50:51]
	v_mov_b64_e32 v[36:37], v[52:53]
	v_mov_b64_e32 v[38:39], v[54:55]
	v_mov_b64_e32 v[40:41], v[56:57]
	v_mov_b64_e32 v[42:43], v[58:59]
	s_add_i32 s38, s3, s30
	s_cmp_gt_i32 s38, 0x83ff
	s_cbranch_scc1 .Lxc_nopf
	s_add_i32 s40, s38, 0xffff8000
	s_cmpk_gt_i32 s38, 0x7fff
	s_cselect_b32 s40, s40, s38
	s_cselect_b32 s42, s36, s34
	s_cselect_b32 s43, s37, s35
	s_ashr_i32 s41, s40, 31
	s_lshl_b64 s[40:41], s[40:41], 12
	s_add_u32 s16, s42, s40
	s_addc_u32 s17, s43, s41
	global_load_dwordx4 v[44:47], v13, s[16:17]
	global_load_dwordx4 v[48:51], v13, s[16:17] offset:1024
	global_load_dwordx4 v[52:55], v13, s[16:17] offset:2048
	global_load_dwordx4 v[56:59], v13, s[16:17] offset:3072
.Lxc_nopf:
	s_add_i32 s8, s3, 0xffff8000
	s_cmpk_gt_i32 s3, 0x7fff
	s_cselect_b32 s9, 8, 0
	s_cselect_b32 s8, s8, s3
	s_cselect_b32 s22, s21, 0x7a00000
	s_ashr_i32 s9, s8, 31
	s_lshl_b64 s[16:17], s[8:9], 12
	s_add_u32 s22, s12, s22
	s_addc_u32 s23, s13, 0
	s_lshl_b64 s[10:11], s[8:9], 11
	s_add_u32 s10, s22, s10
	s_addc_u32 s11, s23, s11
	s_cmp_lt_i32 s3, 0x8000
	v_bfe_u32 v18, v14, 16, 1
	v_bfe_u32 v19, v15, 16, 1
	v_bfe_u32 v21, v17, 16, 1
	v_bfe_u32 v20, v16, 16, 1
	v_add3_u32 v18, v14, v18, s20
	v_add3_u32 v14, v15, v19, s20
	v_add3_u32 v15, v17, v21, s20
	v_add3_u32 v19, v16, v20, s20
	v_and_b32_e32 v20, 0xffff0000, v14
	v_and_b32_e32 v21, 0xffff0000, v15
	v_or_b32_sdwa v14, v20, v18 dst_sel:DWORD dst_unused:UNUSED_PAD src0_sel:DWORD src1_sel:WORD_1
	v_or_b32_sdwa v15, v21, v19 dst_sel:DWORD dst_unused:UNUSED_PAD src0_sel:DWORD src1_sel:WORD_1
	global_store_dwordx2 v2, v[14:15], s[10:11]
	v_and_b32_e32 v18, 0xffff0000, v18
	v_and_b32_e32 v19, 0xffff0000, v19
	v_mul_f32_e32 v20, v20, v20
	v_mul_f32_e32 v21, v21, v21
	v_fmac_f32_e32 v20, v18, v18
	v_fmac_f32_e32 v21, v19, v19
	v_add_f32_e32 v18, v20, v21
	v_mov_b64_e32 v[14:15], v[32:33]
	v_mov_b64_e32 v[16:17], v[34:35]
	v_bfe_u32 v22, v14, 16, 1
	v_bfe_u32 v23, v15, 16, 1
	v_bfe_u32 v25, v17, 16, 1
	v_bfe_u32 v24, v16, 16, 1
	v_add3_u32 v22, v14, v22, s20
	v_add3_u32 v14, v15, v23, s20
	v_add3_u32 v15, v17, v25, s20
	v_add3_u32 v23, v16, v24, s20
	v_and_b32_e32 v24, 0xffff0000, v14
	v_and_b32_e32 v25, 0xffff0000, v15
	v_or_b32_sdwa v14, v24, v22 dst_sel:DWORD dst_unused:UNUSED_PAD src0_sel:DWORD src1_sel:WORD_1
	v_or_b32_sdwa v15, v25, v23 dst_sel:DWORD dst_unused:UNUSED_PAD src0_sel:DWORD src1_sel:WORD_1
	global_store_dwordx2 v2, v[14:15], s[10:11] offset:512
	v_and_b32_e32 v19, 0xffff0000, v22
	v_and_b32_e32 v20, 0xffff0000, v23
	v_mul_f32_e32 v21, v24, v24
	v_mul_f32_e32 v22, v25, v25
	v_fmac_f32_e32 v21, v19, v19
	v_fmac_f32_e32 v22, v20, v20
	v_add_f32_e32 v19, v21, v22
	v_add_f32_e32 v18, v18, v19
	v_mov_b64_e32 v[14:15], v[36:37]
	v_mov_b64_e32 v[16:17], v[38:39]
	v_bfe_u32 v26, v14, 16, 1
	v_bfe_u32 v27, v15, 16, 1
	v_bfe_u32 v29, v17, 16, 1
	v_bfe_u32 v28, v16, 16, 1
	v_add3_u32 v26, v14, v26, s20
	v_add3_u32 v14, v15, v27, s20
	v_add3_u32 v15, v17, v29, s20
	v_add3_u32 v27, v16, v28, s20
	v_and_b32_e32 v28, 0xffff0000, v14
	v_and_b32_e32 v29, 0xffff0000, v15
	v_or_b32_sdwa v14, v28, v26 dst_sel:DWORD dst_unused:UNUSED_PAD src0_sel:DWORD src1_sel:WORD_1
	v_or_b32_sdwa v15, v29, v27 dst_sel:DWORD dst_unused:UNUSED_PAD src0_sel:DWORD src1_sel:WORD_1
	global_store_dwordx2 v2, v[14:15], s[10:11] offset:1024
	v_and_b32_e32 v19, 0xffff0000, v26
	v_and_b32_e32 v20, 0xffff0000, v27
	v_mul_f32_e32 v21, v28, v28
	v_mul_f32_e32 v22, v29, v29
	v_fmac_f32_e32 v21, v19, v19
	v_fmac_f32_e32 v22, v20, v20
	v_add_f32_e32 v19, v21, v22
	v_add_f32_e32 v18, v18, v19
	v_mov_b64_e32 v[14:15], v[40:41]
	v_mov_b64_e32 v[16:17], v[42:43]
	v_bfe_u32 v20, v15, 16, 1
	v_bfe_u32 v22, v17, 16, 1
	v_bfe_u32 v19, v14, 16, 1
	v_bfe_u32 v21, v16, 16, 1
	v_add3_u32 v15, v15, v20, s20
	v_add3_u32 v17, v17, v22, s20
	v_add3_u32 v14, v14, v19, s20
	v_add3_u32 v16, v16, v21, s20
	v_and_b32_e32 v15, 0xffff0000, v15
	v_and_b32_e32 v17, 0xffff0000, v17
	v_and_b32_e32 v19, 0xffff0000, v14
	v_and_b32_e32 v20, 0xffff0000, v16
	v_mul_f32_e32 v21, v15, v15
	v_mul_f32_e32 v22, v17, v17
	v_fmac_f32_e32 v21, v19, v19
	v_fmac_f32_e32 v22, v20, v20
	v_add_f32_e32 v19, v21, v22
	v_add_f32_e32 v18, v18, v19
	v_or_b32_sdwa v14, v15, v14 dst_sel:DWORD dst_unused:UNUSED_PAD src0_sel:DWORD src1_sel:WORD_1
	v_or_b32_sdwa v15, v17, v16 dst_sel:DWORD dst_unused:UNUSED_PAD src0_sel:DWORD src1_sel:WORD_1
	global_store_dwordx2 v2, v[14:15], s[10:11] offset:1536
	s_mov_b64 s[10:11], -1
	s_nop 1
	v_add_f32_dpp v18, v18, v18 quad_perm:[1,0,3,2] row_mask:0xf bank_mask:0xf
	s_nop 1
	v_add_f32_dpp v18, v18, v18 quad_perm:[2,3,0,1] row_mask:0xf bank_mask:0xf
	s_nop 1
	v_add_f32_dpp v18, v18, v18 row_half_mirror row_mask:0xf bank_mask:0xf
	s_nop 1
	v_add_f32_dpp v18, v18, v18 row_mirror row_mask:0xf bank_mask:0xf
	v_mov_b32_e32 v19, v18
	s_nop 1
	v_permlane16_swap_b32_e32 v19, v18
	v_add_f32_e32 v18, v18, v19
	v_mov_b32_e32 v19, v18
	s_nop 1
	v_permlane32_swap_b32_e32 v19, v18
	v_add_f32_e32 v14, v18, v19
	s_cbranch_scc1 .LBB0_357
	s_andn2_b64 vcc, exec, s[10:11]
	s_cbranch_vccnz .LBB0_354
	s_branch .LBB0_360
